# carry folded into conv|F tail; conv rows split 8 per wave on the carry workgroups, 14 (layer 0) / 12 (layer 1) on the others
# speedup vs baseline: 1.0039x; 1.0039x over previous
; __device__ __forceinline__ void phase_conv(Frame& F, int l, int nblk) {
;     ...
;     const int nrows = l == 0 ? MT : ML, nwv = nblk * NWAVES, rpw = (nrows + nwv - 1) / nwv, r_lo = (F.vcu * NWAVES + F.wave) * rpw, r_hi = r_lo + rpw < nrows ? r_lo + rpw : nrows;
;     if (r_lo >= r_hi) return;
.LBB0_429:
	s_lshl_b32 s0, s14, 3
	s_abs_i32 s1, s0
	v_cvt_f32_u32_e32 v1, s1
	s_add_i32 s3, s0, 0x47ff
	s_sub_i32 s4, 0xffffb801, s0
	s_xor_b32 s0, s3, s0
	v_rcp_iflag_f32_e32 v1, v1
	s_max_i32 s3, s3, s4
	s_sub_i32 s4, 0, s1
	s_ashr_i32 s2, s13, 6
	v_mul_f32_e32 v1, 0x4f7ffffe, v1
	v_cvt_u32_f32_e32 v1, v1
	s_ashr_i32 s0, s0, 31
	v_readfirstlane_b32 s5, v1
	s_mul_i32 s4, s4, s5
	s_mul_hi_u32 s4, s5, s4
	s_add_i32 s5, s5, s4
	s_mul_hi_u32 s4, s3, s5
	s_mul_i32 s5, s4, s1
	s_sub_i32 s3, s3, s5
	s_add_i32 s6, s4, 1
	s_sub_i32 s5, s3, s1
	s_cmp_ge_u32 s3, s1
	s_cselect_b32 s4, s6, s4
	s_cselect_b32 s3, s5, s3
	s_add_i32 s5, s4, 1
	s_cmp_ge_u32 s3, s1
	s_cselect_b32 s1, s5, s4
	s_xor_b32 s1, s1, s0
	s_sub_i32 s0, s1, s0
	s_lshl_b32 s1, s12, 3
	s_add_i32 s1, s1, s2
	s_cmp_lt_u32 s1, 0x200
	s_cbranch_scc1 .Lcv0_a
	s_mov_b32 s0, 14
	s_sub_i32 s1, s1, 0x200
	s_mul_i32 s2, s0, s1
	s_add_i32 s2, s2, 4096
	s_branch .Lcv0_j
.Lcv0_a:
	s_mov_b32 s0, 8
	s_mul_i32 s2, s0, s1

; __device__ __forceinline__ void phase_conv(Frame& F, int l, int nblk) {
;     ...
;     const int nrows = l == 0 ? MT : ML, nwv = nblk * NWAVES, rpw = (nrows + nwv - 1) / nwv, r_lo = (F.vcu * NWAVES + F.wave) * rpw, r_hi = r_lo + rpw < nrows ? r_lo + rpw : nrows;
;     if (r_lo >= r_hi) return;
.LBB0_1449:
	s_lshl_b32 s0, s14, 3
	s_abs_i32 s1, s0
	v_cvt_f32_u32_e32 v1, s1
	s_add_i32 s3, s0, 0x3fff
	s_sub_i32 s4, 0xffffc001, s0
	s_xor_b32 s0, s3, s0
	v_rcp_iflag_f32_e32 v1, v1
	s_max_i32 s3, s3, s4
	s_sub_i32 s4, 0, s1
	s_ashr_i32 s2, s13, 6
	v_mul_f32_e32 v1, 0x4f7ffffe, v1
	v_cvt_u32_f32_e32 v1, v1
	s_ashr_i32 s0, s0, 31
	v_readfirstlane_b32 s5, v1
	s_mul_i32 s4, s4, s5
	s_mul_hi_u32 s4, s5, s4
	s_add_i32 s5, s5, s4
	s_mul_hi_u32 s4, s3, s5
	s_mul_i32 s5, s4, s1
	s_sub_i32 s3, s3, s5
	s_add_i32 s6, s4, 1
	s_sub_i32 s5, s3, s1
	s_cmp_ge_u32 s3, s1
	s_cselect_b32 s4, s6, s4
	s_cselect_b32 s3, s5, s3
	s_add_i32 s5, s4, 1
	s_cmp_ge_u32 s3, s1
	s_cselect_b32 s1, s5, s4
	s_xor_b32 s1, s1, s0
	s_sub_i32 s0, s1, s0
	s_lshl_b32 s1, s12, 3
	s_add_i32 s1, s1, s2
	s_cmp_lt_u32 s1, 0x200
	s_cbranch_scc1 .Lcv1_a
	s_mov_b32 s0, 12
	s_sub_i32 s1, s1, 0x200
	s_mul_i32 s2, s0, s1
	s_add_i32 s2, s2, 4096
	s_branch .Lcv1_j
